# top-k gt emission: redundant exec re-save between the two 4-site half batches of a chunk removed (16 SALU ops per query)
# speedup vs baseline: 1.0089x; 1.0089x over previous
.LBB0_1259:
	s_nop 0
	s_nop 0
	s_nop 0
	s_nop 0
	s_nop 0
	s_nop 0
	s_nop 0
	s_nop 0
	s_nop 0
	s_nop 0
	s_nop 0
	s_nop 0
	s_nop 0
	s_nop 0
	s_nop 0
	s_nop 0
	s_nop 0
	s_nop 0
	s_nop 0
	s_nop 0
	s_nop 0
	s_nop 0
	s_nop 0
	s_nop 0
	s_nop 0
	s_nop 0
	s_nop 0
	s_nop 0
	s_nop 0
	s_nop 0
	s_nop 0
	s_nop 0
	s_nop 0
	s_nop 0
	s_nop 0
	s_nop 0
	s_nop 0
	s_nop 0
	s_nop 0
	s_nop 0
	s_nop 0
	s_nop 0
	s_nop 0
	s_nop 0
	s_nop 0
	s_nop 0
	s_nop 0
	s_nop 0
	s_nop 0
	s_nop 0
	s_nop 0
	s_nop 0
	s_nop 0
	s_nop 0
	s_nop 0
	s_nop 0
	s_cmp_gt_i32 s14, 0
	s_cselect_b64 s[42:43], -1, 0
	s_cmp_lt_i32 s14, 1
	s_mov_b32 s4, 0
	s_cbranch_scc1 .LBB0_1277
	s_mov_b64 s[34:35], exec
	v_cmp_gt_u32_sdwa s[70:71], v50, v66 src0_sel:WORD_0 src1_sel:DWORD
	v_cmp_gt_u32_sdwa s[88:89], v50, v66 src0_sel:WORD_1 src1_sel:DWORD
	v_cmp_gt_u32_sdwa s[90:91], v51, v66 src0_sel:WORD_0 src1_sel:DWORD
	v_cmp_gt_u32_sdwa s[94:95], v51, v66 src0_sel:WORD_1 src1_sel:DWORD
	s_lshl1_add_u32 s32, s4, s52
	v_mbcnt_lo_u32_b32 v67, s70, 0
	v_mbcnt_lo_u32_b32 v68, s88, 0
	v_mbcnt_lo_u32_b32 v69, s90, 0
	v_mbcnt_lo_u32_b32 v70, s94, 0
	s_bcnt1_i32_b64 s93, s[70:71]
	s_add_i32 s4, s4, s93
	s_lshl1_add_u32 s85, s4, s52
	v_mbcnt_hi_u32_b32 v67, s71, v67
	s_bcnt1_i32_b64 s93, s[88:89]
	s_add_i32 s4, s4, s93
	s_lshl1_add_u32 s86, s4, s52
	v_mbcnt_hi_u32_b32 v68, s89, v68
	s_bcnt1_i32_b64 s93, s[90:91]
	s_add_i32 s4, s4, s93
	s_lshl1_add_u32 s15, s4, s52
	v_mbcnt_hi_u32_b32 v69, s91, v69
	s_bcnt1_i32_b64 s93, s[94:95]
	s_add_i32 s4, s4, s93
	v_mbcnt_hi_u32_b32 v70, s95, v70
	v_lshl_add_u32 v67, v67, 1, s32
	v_lshl_add_u32 v68, v68, 1, s85
	v_lshl_add_u32 v69, v69, 1, s86
	v_lshl_add_u32 v70, v70, 1, s15
	s_mov_b64 exec, s[70:71]
	ds_write_b16 v67, v119 offset:32768
	s_mov_b64 exec, s[88:89]
	ds_write_b16 v68, v120 offset:32768
	s_mov_b64 exec, s[90:91]
	ds_write_b16 v69, v121 offset:32768
	s_mov_b64 exec, s[94:95]
	ds_write_b16 v70, v122 offset:32768
	s_mov_b64 exec, s[34:35]
	v_cmp_gt_u32_sdwa s[70:71], v52, v66 src0_sel:WORD_0 src1_sel:DWORD
	v_cmp_gt_u32_sdwa s[88:89], v52, v66 src0_sel:WORD_1 src1_sel:DWORD
	v_cmp_gt_u32_sdwa s[90:91], v53, v66 src0_sel:WORD_0 src1_sel:DWORD
	v_cmp_gt_u32_sdwa s[94:95], v53, v66 src0_sel:WORD_1 src1_sel:DWORD
	s_lshl1_add_u32 s32, s4, s52
	v_mbcnt_lo_u32_b32 v67, s70, 0
	v_mbcnt_lo_u32_b32 v68, s88, 0
	v_mbcnt_lo_u32_b32 v69, s90, 0
	v_mbcnt_lo_u32_b32 v70, s94, 0
	s_bcnt1_i32_b64 s93, s[70:71]
	s_add_i32 s4, s4, s93
	s_lshl1_add_u32 s85, s4, s52
	v_mbcnt_hi_u32_b32 v67, s71, v67
	s_bcnt1_i32_b64 s93, s[88:89]
	s_add_i32 s4, s4, s93
	s_lshl1_add_u32 s86, s4, s52
	v_mbcnt_hi_u32_b32 v68, s89, v68
	s_bcnt1_i32_b64 s93, s[90:91]
	s_add_i32 s4, s4, s93
	s_lshl1_add_u32 s15, s4, s52
	v_mbcnt_hi_u32_b32 v69, s91, v69
	s_bcnt1_i32_b64 s93, s[94:95]
	s_add_i32 s4, s4, s93
	v_mbcnt_hi_u32_b32 v70, s95, v70
	v_lshl_add_u32 v67, v67, 1, s32
	v_lshl_add_u32 v68, v68, 1, s85
	v_lshl_add_u32 v69, v69, 1, s86
	v_lshl_add_u32 v70, v70, 1, s15
	s_mov_b64 exec, s[70:71]
	ds_write_b16 v67, v123 offset:32768
	s_mov_b64 exec, s[88:89]
	ds_write_b16 v68, v124 offset:32768
	s_mov_b64 exec, s[90:91]
	ds_write_b16 v69, v125 offset:32768
	s_mov_b64 exec, s[94:95]
	ds_write_b16 v70, v126 offset:32768
	s_mov_b64 exec, s[34:35]

.LBB0_1292:
	s_mov_b64 s[34:35], exec
	v_cmp_gt_u32_sdwa s[70:71], v38, v66 src0_sel:WORD_0 src1_sel:DWORD
	v_cmp_gt_u32_sdwa s[88:89], v38, v66 src0_sel:WORD_1 src1_sel:DWORD
	v_cmp_gt_u32_sdwa s[90:91], v39, v66 src0_sel:WORD_0 src1_sel:DWORD
	v_cmp_gt_u32_sdwa s[94:95], v39, v66 src0_sel:WORD_1 src1_sel:DWORD
	s_lshl1_add_u32 s32, s4, s52
	v_mbcnt_lo_u32_b32 v67, s70, 0
	v_mbcnt_lo_u32_b32 v68, s88, 0
	v_mbcnt_lo_u32_b32 v69, s90, 0
	v_mbcnt_lo_u32_b32 v70, s94, 0
	s_bcnt1_i32_b64 s93, s[70:71]
	s_add_i32 s4, s4, s93
	s_lshl1_add_u32 s85, s4, s52
	v_mbcnt_hi_u32_b32 v67, s71, v67
	s_bcnt1_i32_b64 s93, s[88:89]
	s_add_i32 s4, s4, s93
	s_lshl1_add_u32 s86, s4, s52
	v_mbcnt_hi_u32_b32 v68, s89, v68
	s_bcnt1_i32_b64 s93, s[90:91]
	s_add_i32 s4, s4, s93
	s_lshl1_add_u32 s15, s4, s52
	v_mbcnt_hi_u32_b32 v69, s91, v69
	s_bcnt1_i32_b64 s93, s[94:95]
	s_add_i32 s4, s4, s93
	v_mbcnt_hi_u32_b32 v70, s95, v70
	v_or_b32_e32 v71, 0x200, v119
	v_or_b32_e32 v72, 0x201, v119
	v_or_b32_e32 v73, 0x202, v119
	v_or_b32_e32 v74, 0x203, v119
	v_lshl_add_u32 v67, v67, 1, s32
	v_lshl_add_u32 v68, v68, 1, s85
	v_lshl_add_u32 v69, v69, 1, s86
	v_lshl_add_u32 v70, v70, 1, s15
	s_mov_b64 exec, s[70:71]
	ds_write_b16 v67, v71 offset:32768
	s_mov_b64 exec, s[88:89]
	ds_write_b16 v68, v72 offset:32768
	s_mov_b64 exec, s[90:91]
	ds_write_b16 v69, v73 offset:32768
	s_mov_b64 exec, s[94:95]
	ds_write_b16 v70, v74 offset:32768
	s_mov_b64 exec, s[34:35]
	v_cmp_gt_u32_sdwa s[70:71], v40, v66 src0_sel:WORD_0 src1_sel:DWORD
	v_cmp_gt_u32_sdwa s[88:89], v40, v66 src0_sel:WORD_1 src1_sel:DWORD
	v_cmp_gt_u32_sdwa s[90:91], v41, v66 src0_sel:WORD_0 src1_sel:DWORD
	v_cmp_gt_u32_sdwa s[94:95], v41, v66 src0_sel:WORD_1 src1_sel:DWORD
	s_lshl1_add_u32 s32, s4, s52
	v_mbcnt_lo_u32_b32 v67, s70, 0
	v_mbcnt_lo_u32_b32 v68, s88, 0
	v_mbcnt_lo_u32_b32 v69, s90, 0
	v_mbcnt_lo_u32_b32 v70, s94, 0
	s_bcnt1_i32_b64 s93, s[70:71]
	s_add_i32 s4, s4, s93
	s_lshl1_add_u32 s85, s4, s52
	v_mbcnt_hi_u32_b32 v67, s71, v67
	s_bcnt1_i32_b64 s93, s[88:89]
	s_add_i32 s4, s4, s93
	s_lshl1_add_u32 s86, s4, s52
	v_mbcnt_hi_u32_b32 v68, s89, v68
	s_bcnt1_i32_b64 s93, s[90:91]
	s_add_i32 s4, s4, s93
	s_lshl1_add_u32 s15, s4, s52
	v_mbcnt_hi_u32_b32 v69, s91, v69
	s_bcnt1_i32_b64 s93, s[94:95]
	s_add_i32 s4, s4, s93
	v_mbcnt_hi_u32_b32 v70, s95, v70
	v_or_b32_e32 v71, 0x204, v119
	v_or_b32_e32 v72, 0x205, v119
	v_or_b32_e32 v73, 0x206, v119
	v_or_b32_e32 v74, 0x207, v119
	v_lshl_add_u32 v67, v67, 1, s32
	v_lshl_add_u32 v68, v68, 1, s85
	v_lshl_add_u32 v69, v69, 1, s86
	v_lshl_add_u32 v70, v70, 1, s15
	s_mov_b64 exec, s[70:71]
	ds_write_b16 v67, v71 offset:32768
	s_mov_b64 exec, s[88:89]
	ds_write_b16 v68, v72 offset:32768
	s_mov_b64 exec, s[90:91]
	ds_write_b16 v69, v73 offset:32768
	s_mov_b64 exec, s[94:95]
	ds_write_b16 v70, v74 offset:32768
	s_mov_b64 exec, s[34:35]
	s_cmp_gt_i32 s14, 2
	s_cselect_b64 s[74:75], -1, 0
	s_cmp_lt_i32 s14, 3
	s_cbranch_scc1 .LBB0_1279
.LBB0_1309:
	s_mov_b64 s[34:35], exec
	v_cmp_gt_u32_sdwa s[70:71], v26, v66 src0_sel:WORD_0 src1_sel:DWORD
	v_cmp_gt_u32_sdwa s[88:89], v26, v66 src0_sel:WORD_1 src1_sel:DWORD
	v_cmp_gt_u32_sdwa s[90:91], v27, v66 src0_sel:WORD_0 src1_sel:DWORD
	v_cmp_gt_u32_sdwa s[94:95], v27, v66 src0_sel:WORD_1 src1_sel:DWORD
	s_lshl1_add_u32 s32, s4, s52
	v_mbcnt_lo_u32_b32 v67, s70, 0
	v_mbcnt_lo_u32_b32 v68, s88, 0
	v_mbcnt_lo_u32_b32 v69, s90, 0
	v_mbcnt_lo_u32_b32 v70, s94, 0
	s_bcnt1_i32_b64 s93, s[70:71]
	s_add_i32 s4, s4, s93
	s_lshl1_add_u32 s85, s4, s52
	v_mbcnt_hi_u32_b32 v67, s71, v67
	s_bcnt1_i32_b64 s93, s[88:89]
	s_add_i32 s4, s4, s93
	s_lshl1_add_u32 s86, s4, s52
	v_mbcnt_hi_u32_b32 v68, s89, v68
	s_bcnt1_i32_b64 s93, s[90:91]
	s_add_i32 s4, s4, s93
	s_lshl1_add_u32 s15, s4, s52
	v_mbcnt_hi_u32_b32 v69, s91, v69
	s_bcnt1_i32_b64 s93, s[94:95]
	s_add_i32 s4, s4, s93
	v_mbcnt_hi_u32_b32 v70, s95, v70
	v_or_b32_e32 v71, 0x400, v119
	v_or_b32_e32 v72, 0x401, v119
	v_or_b32_e32 v73, 0x402, v119
	v_or_b32_e32 v74, 0x403, v119
	v_lshl_add_u32 v67, v67, 1, s32
	v_lshl_add_u32 v68, v68, 1, s85
	v_lshl_add_u32 v69, v69, 1, s86
	v_lshl_add_u32 v70, v70, 1, s15
	s_mov_b64 exec, s[70:71]
	ds_write_b16 v67, v71 offset:32768
	s_mov_b64 exec, s[88:89]
	ds_write_b16 v68, v72 offset:32768
	s_mov_b64 exec, s[90:91]
	ds_write_b16 v69, v73 offset:32768
	s_mov_b64 exec, s[94:95]
	ds_write_b16 v70, v74 offset:32768
	s_mov_b64 exec, s[34:35]
	v_cmp_gt_u32_sdwa s[70:71], v28, v66 src0_sel:WORD_0 src1_sel:DWORD
	v_cmp_gt_u32_sdwa s[88:89], v28, v66 src0_sel:WORD_1 src1_sel:DWORD
	v_cmp_gt_u32_sdwa s[90:91], v29, v66 src0_sel:WORD_0 src1_sel:DWORD
	v_cmp_gt_u32_sdwa s[94:95], v29, v66 src0_sel:WORD_1 src1_sel:DWORD
	s_lshl1_add_u32 s32, s4, s52
	v_mbcnt_lo_u32_b32 v67, s70, 0
	v_mbcnt_lo_u32_b32 v68, s88, 0
	v_mbcnt_lo_u32_b32 v69, s90, 0
	v_mbcnt_lo_u32_b32 v70, s94, 0
	s_bcnt1_i32_b64 s93, s[70:71]
	s_add_i32 s4, s4, s93
	s_lshl1_add_u32 s85, s4, s52
	v_mbcnt_hi_u32_b32 v67, s71, v67
	s_bcnt1_i32_b64 s93, s[88:89]
	s_add_i32 s4, s4, s93
	s_lshl1_add_u32 s86, s4, s52
	v_mbcnt_hi_u32_b32 v68, s89, v68
	s_bcnt1_i32_b64 s93, s[90:91]
	s_add_i32 s4, s4, s93
	s_lshl1_add_u32 s15, s4, s52
	v_mbcnt_hi_u32_b32 v69, s91, v69
	s_bcnt1_i32_b64 s93, s[94:95]
	s_add_i32 s4, s4, s93
	v_mbcnt_hi_u32_b32 v70, s95, v70
	v_or_b32_e32 v71, 0x404, v119
	v_or_b32_e32 v72, 0x405, v119
	v_or_b32_e32 v73, 0x406, v119
	v_or_b32_e32 v74, 0x407, v119
	v_lshl_add_u32 v67, v67, 1, s32
	v_lshl_add_u32 v68, v68, 1, s85
	v_lshl_add_u32 v69, v69, 1, s86
	v_lshl_add_u32 v70, v70, 1, s15
	s_mov_b64 exec, s[70:71]
	ds_write_b16 v67, v71 offset:32768
	s_mov_b64 exec, s[88:89]
	ds_write_b16 v68, v72 offset:32768
	s_mov_b64 exec, s[90:91]
	ds_write_b16 v69, v73 offset:32768
	s_mov_b64 exec, s[94:95]
	ds_write_b16 v70, v74 offset:32768
	s_mov_b64 exec, s[34:35]
	s_cmp_gt_i32 s14, 3
	s_cselect_b64 s[68:69], -1, 0
	s_cmp_lt_i32 s14, 4
	s_cbranch_scc1 .LBB0_1280
.LBB0_1326:
	s_mov_b64 s[34:35], exec
	v_cmp_gt_u32_sdwa s[70:71], v18, v66 src0_sel:WORD_0 src1_sel:DWORD
	v_cmp_gt_u32_sdwa s[88:89], v18, v66 src0_sel:WORD_1 src1_sel:DWORD
	v_cmp_gt_u32_sdwa s[90:91], v19, v66 src0_sel:WORD_0 src1_sel:DWORD
	v_cmp_gt_u32_sdwa s[94:95], v19, v66 src0_sel:WORD_1 src1_sel:DWORD
	s_lshl1_add_u32 s32, s4, s52
	v_mbcnt_lo_u32_b32 v67, s70, 0
	v_mbcnt_lo_u32_b32 v68, s88, 0
	v_mbcnt_lo_u32_b32 v69, s90, 0
	v_mbcnt_lo_u32_b32 v70, s94, 0
	s_bcnt1_i32_b64 s93, s[70:71]
	s_add_i32 s4, s4, s93
	s_lshl1_add_u32 s85, s4, s52
	v_mbcnt_hi_u32_b32 v67, s71, v67
	s_bcnt1_i32_b64 s93, s[88:89]
	s_add_i32 s4, s4, s93
	s_lshl1_add_u32 s86, s4, s52
	v_mbcnt_hi_u32_b32 v68, s89, v68
	s_bcnt1_i32_b64 s93, s[90:91]
	s_add_i32 s4, s4, s93
	s_lshl1_add_u32 s15, s4, s52
	v_mbcnt_hi_u32_b32 v69, s91, v69
	s_bcnt1_i32_b64 s93, s[94:95]
	s_add_i32 s4, s4, s93
	v_mbcnt_hi_u32_b32 v70, s95, v70
	v_or_b32_e32 v71, 0x600, v119
	v_or_b32_e32 v72, 0x601, v119
	v_or_b32_e32 v73, 0x602, v119
	v_or_b32_e32 v74, 0x603, v119
	v_lshl_add_u32 v67, v67, 1, s32
	v_lshl_add_u32 v68, v68, 1, s85
	v_lshl_add_u32 v69, v69, 1, s86
	v_lshl_add_u32 v70, v70, 1, s15
	s_mov_b64 exec, s[70:71]
	ds_write_b16 v67, v71 offset:32768
	s_mov_b64 exec, s[88:89]
	ds_write_b16 v68, v72 offset:32768
	s_mov_b64 exec, s[90:91]
	ds_write_b16 v69, v73 offset:32768
	s_mov_b64 exec, s[94:95]
	ds_write_b16 v70, v74 offset:32768
	s_mov_b64 exec, s[34:35]
	v_cmp_gt_u32_sdwa s[70:71], v20, v66 src0_sel:WORD_0 src1_sel:DWORD
	v_cmp_gt_u32_sdwa s[88:89], v20, v66 src0_sel:WORD_1 src1_sel:DWORD
	v_cmp_gt_u32_sdwa s[90:91], v21, v66 src0_sel:WORD_0 src1_sel:DWORD
	v_cmp_gt_u32_sdwa s[94:95], v21, v66 src0_sel:WORD_1 src1_sel:DWORD
	s_lshl1_add_u32 s32, s4, s52
	v_mbcnt_lo_u32_b32 v67, s70, 0
	v_mbcnt_lo_u32_b32 v68, s88, 0
	v_mbcnt_lo_u32_b32 v69, s90, 0
	v_mbcnt_lo_u32_b32 v70, s94, 0
	s_bcnt1_i32_b64 s93, s[70:71]
	s_add_i32 s4, s4, s93
	s_lshl1_add_u32 s85, s4, s52
	v_mbcnt_hi_u32_b32 v67, s71, v67
	s_bcnt1_i32_b64 s93, s[88:89]
	s_add_i32 s4, s4, s93
	s_lshl1_add_u32 s86, s4, s52
	v_mbcnt_hi_u32_b32 v68, s89, v68
	s_bcnt1_i32_b64 s93, s[90:91]
	s_add_i32 s4, s4, s93
	s_lshl1_add_u32 s15, s4, s52
	v_mbcnt_hi_u32_b32 v69, s91, v69
	s_bcnt1_i32_b64 s93, s[94:95]
	s_add_i32 s4, s4, s93
	v_mbcnt_hi_u32_b32 v70, s95, v70
	v_or_b32_e32 v71, 0x604, v119
	v_or_b32_e32 v72, 0x605, v119
	v_or_b32_e32 v73, 0x606, v119
	v_or_b32_e32 v74, 0x607, v119
	v_lshl_add_u32 v67, v67, 1, s32
	v_lshl_add_u32 v68, v68, 1, s85
	v_lshl_add_u32 v69, v69, 1, s86
	v_lshl_add_u32 v70, v70, 1, s15
	s_mov_b64 exec, s[70:71]
	ds_write_b16 v67, v71 offset:32768
	s_mov_b64 exec, s[88:89]
	ds_write_b16 v68, v72 offset:32768
	s_mov_b64 exec, s[90:91]
	ds_write_b16 v69, v73 offset:32768
	s_mov_b64 exec, s[94:95]
	ds_write_b16 v70, v74 offset:32768
	s_mov_b64 exec, s[34:35]
	s_and_b64 vcc, exec, s[8:9]
	s_cbranch_vccnz .LBB0_1281
.LBB0_1343:
	s_mov_b64 s[30:31], exec
	v_cmp_gt_u32_sdwa s[70:71], v58, v66 src0_sel:WORD_0 src1_sel:DWORD
	v_cmp_gt_u32_sdwa s[88:89], v58, v66 src0_sel:WORD_1 src1_sel:DWORD
	v_cmp_gt_u32_sdwa s[90:91], v59, v66 src0_sel:WORD_0 src1_sel:DWORD
	v_cmp_gt_u32_sdwa s[94:95], v59, v66 src0_sel:WORD_1 src1_sel:DWORD
	s_lshl1_add_u32 s32, s4, s52
	v_mbcnt_lo_u32_b32 v67, s70, 0
	v_mbcnt_lo_u32_b32 v68, s88, 0
	v_mbcnt_lo_u32_b32 v69, s90, 0
	v_mbcnt_lo_u32_b32 v70, s94, 0
	s_bcnt1_i32_b64 s93, s[70:71]
	s_add_i32 s4, s4, s93
	s_lshl1_add_u32 s85, s4, s52
	v_mbcnt_hi_u32_b32 v67, s71, v67
	s_bcnt1_i32_b64 s93, s[88:89]
	s_add_i32 s4, s4, s93
	s_lshl1_add_u32 s86, s4, s52
	v_mbcnt_hi_u32_b32 v68, s89, v68
	s_bcnt1_i32_b64 s93, s[90:91]
	s_add_i32 s4, s4, s93
	s_lshl1_add_u32 s15, s4, s52
	v_mbcnt_hi_u32_b32 v69, s91, v69
	s_bcnt1_i32_b64 s93, s[94:95]
	s_add_i32 s4, s4, s93
	v_mbcnt_hi_u32_b32 v70, s95, v70
	v_or_b32_e32 v71, 0x800, v119
	v_lshl_add_u32 v67, v67, 1, s32
	v_lshl_add_u32 v68, v68, 1, s85
	v_lshl_add_u32 v69, v69, 1, s86
	v_lshl_add_u32 v70, v70, 1, s15
	s_mov_b64 exec, s[70:71]
	ds_write_b16 v67, v71 offset:32768
	s_mov_b64 exec, s[88:89]
	ds_write_b16 v68, v152 offset:32768
	s_mov_b64 exec, s[90:91]
	ds_write_b16 v69, v153 offset:32768
	s_mov_b64 exec, s[94:95]
	ds_write_b16 v70, v154 offset:32768
	s_mov_b64 exec, s[30:31]
	v_cmp_gt_u32_sdwa s[70:71], v60, v66 src0_sel:WORD_0 src1_sel:DWORD
	v_cmp_gt_u32_sdwa s[88:89], v60, v66 src0_sel:WORD_1 src1_sel:DWORD
	v_cmp_gt_u32_sdwa s[90:91], v61, v66 src0_sel:WORD_0 src1_sel:DWORD
	v_cmp_gt_u32_sdwa s[94:95], v61, v66 src0_sel:WORD_1 src1_sel:DWORD
	s_lshl1_add_u32 s32, s4, s52
	v_mbcnt_lo_u32_b32 v67, s70, 0
	v_mbcnt_lo_u32_b32 v68, s88, 0
	v_mbcnt_lo_u32_b32 v69, s90, 0
	v_mbcnt_lo_u32_b32 v70, s94, 0
	s_bcnt1_i32_b64 s93, s[70:71]
	s_add_i32 s4, s4, s93
	s_lshl1_add_u32 s85, s4, s52
	v_mbcnt_hi_u32_b32 v67, s71, v67
	s_bcnt1_i32_b64 s93, s[88:89]
	s_add_i32 s4, s4, s93
	s_lshl1_add_u32 s86, s4, s52
	v_mbcnt_hi_u32_b32 v68, s89, v68
	s_bcnt1_i32_b64 s93, s[90:91]
	s_add_i32 s4, s4, s93
	s_lshl1_add_u32 s15, s4, s52
	v_mbcnt_hi_u32_b32 v69, s91, v69
	s_bcnt1_i32_b64 s93, s[94:95]
	s_add_i32 s4, s4, s93
	v_mbcnt_hi_u32_b32 v70, s95, v70
	v_lshl_add_u32 v67, v67, 1, s32
	v_lshl_add_u32 v68, v68, 1, s85
	v_lshl_add_u32 v69, v69, 1, s86
	v_lshl_add_u32 v70, v70, 1, s15
	s_mov_b64 exec, s[70:71]
	ds_write_b16 v67, v155 offset:32768
	s_mov_b64 exec, s[88:89]
	ds_write_b16 v68, v156 offset:32768
	s_mov_b64 exec, s[90:91]
	ds_write_b16 v69, v157 offset:32768
	s_mov_b64 exec, s[94:95]
	ds_write_b16 v70, v158 offset:32768
	s_mov_b64 exec, s[30:31]
	s_cmp_gt_i32 s14, 5
	s_cselect_b64 s[66:67], -1, 0
	s_cmp_lt_i32 s14, 6
	s_cbranch_scc1 .LBB0_1282
.LBB0_1360:
	s_mov_b64 s[30:31], exec
	v_cmp_gt_u32_sdwa s[70:71], v46, v66 src0_sel:WORD_0 src1_sel:DWORD
	v_cmp_gt_u32_sdwa s[88:89], v46, v66 src0_sel:WORD_1 src1_sel:DWORD
	v_cmp_gt_u32_sdwa s[90:91], v47, v66 src0_sel:WORD_0 src1_sel:DWORD
	v_cmp_gt_u32_sdwa s[94:95], v47, v66 src0_sel:WORD_1 src1_sel:DWORD
	s_lshl1_add_u32 s32, s4, s52
	v_mbcnt_lo_u32_b32 v67, s70, 0
	v_mbcnt_lo_u32_b32 v68, s88, 0
	v_mbcnt_lo_u32_b32 v69, s90, 0
	v_mbcnt_lo_u32_b32 v70, s94, 0
	s_bcnt1_i32_b64 s93, s[70:71]
	s_add_i32 s4, s4, s93
	s_lshl1_add_u32 s85, s4, s52
	v_mbcnt_hi_u32_b32 v67, s71, v67
	s_bcnt1_i32_b64 s93, s[88:89]
	s_add_i32 s4, s4, s93
	s_lshl1_add_u32 s86, s4, s52
	v_mbcnt_hi_u32_b32 v68, s89, v68
	s_bcnt1_i32_b64 s93, s[90:91]
	s_add_i32 s4, s4, s93
	s_lshl1_add_u32 s15, s4, s52
	v_mbcnt_hi_u32_b32 v69, s91, v69
	s_bcnt1_i32_b64 s93, s[94:95]
	s_add_i32 s4, s4, s93
	v_mbcnt_hi_u32_b32 v70, s95, v70
	v_lshl_add_u32 v67, v67, 1, s32
	v_lshl_add_u32 v68, v68, 1, s85
	v_lshl_add_u32 v69, v69, 1, s86
	v_lshl_add_u32 v70, v70, 1, s15
	s_mov_b64 exec, s[70:71]
	ds_write_b16 v67, v159 offset:32768
	s_mov_b64 exec, s[88:89]
	ds_write_b16 v68, v160 offset:32768
	s_mov_b64 exec, s[90:91]
	ds_write_b16 v69, v161 offset:32768
	s_mov_b64 exec, s[94:95]
	ds_write_b16 v70, v162 offset:32768
	s_mov_b64 exec, s[30:31]
	v_cmp_gt_u32_sdwa s[70:71], v48, v66 src0_sel:WORD_0 src1_sel:DWORD
	v_cmp_gt_u32_sdwa s[88:89], v48, v66 src0_sel:WORD_1 src1_sel:DWORD
	v_cmp_gt_u32_sdwa s[90:91], v49, v66 src0_sel:WORD_0 src1_sel:DWORD
	v_cmp_gt_u32_sdwa s[94:95], v49, v66 src0_sel:WORD_1 src1_sel:DWORD
	s_lshl1_add_u32 s32, s4, s52
	v_mbcnt_lo_u32_b32 v67, s70, 0
	v_mbcnt_lo_u32_b32 v68, s88, 0
	v_mbcnt_lo_u32_b32 v69, s90, 0
	v_mbcnt_lo_u32_b32 v70, s94, 0
	s_bcnt1_i32_b64 s93, s[70:71]
	s_add_i32 s4, s4, s93
	s_lshl1_add_u32 s85, s4, s52
	v_mbcnt_hi_u32_b32 v67, s71, v67
	s_bcnt1_i32_b64 s93, s[88:89]
	s_add_i32 s4, s4, s93
	s_lshl1_add_u32 s86, s4, s52
	v_mbcnt_hi_u32_b32 v68, s89, v68
	s_bcnt1_i32_b64 s93, s[90:91]
	s_add_i32 s4, s4, s93
	s_lshl1_add_u32 s15, s4, s52
	v_mbcnt_hi_u32_b32 v69, s91, v69
	s_bcnt1_i32_b64 s93, s[94:95]
	s_add_i32 s4, s4, s93
	v_mbcnt_hi_u32_b32 v70, s95, v70
	v_lshl_add_u32 v67, v67, 1, s32
	v_lshl_add_u32 v68, v68, 1, s85
	v_lshl_add_u32 v69, v69, 1, s86
	v_lshl_add_u32 v70, v70, 1, s15
	s_mov_b64 exec, s[70:71]
	ds_write_b16 v67, v163 offset:32768
	s_mov_b64 exec, s[88:89]
	ds_write_b16 v68, v164 offset:32768
	s_mov_b64 exec, s[90:91]
	ds_write_b16 v69, v165 offset:32768
	s_mov_b64 exec, s[94:95]
	ds_write_b16 v70, v166 offset:32768
	s_mov_b64 exec, s[30:31]
	s_cmp_gt_i32 s14, 6
	s_cselect_b64 s[64:65], -1, 0
	s_cmp_lt_i32 s14, 7
	s_cbranch_scc1 .LBB0_1283
.LBB0_1377:
	s_mov_b64 s[30:31], exec
	v_cmp_gt_u32_sdwa s[70:71], v34, v66 src0_sel:WORD_0 src1_sel:DWORD
	v_cmp_gt_u32_sdwa s[88:89], v34, v66 src0_sel:WORD_1 src1_sel:DWORD
	v_cmp_gt_u32_sdwa s[90:91], v35, v66 src0_sel:WORD_0 src1_sel:DWORD
	v_cmp_gt_u32_sdwa s[94:95], v35, v66 src0_sel:WORD_1 src1_sel:DWORD
	s_lshl1_add_u32 s32, s4, s52
	v_mbcnt_lo_u32_b32 v67, s70, 0
	v_mbcnt_lo_u32_b32 v68, s88, 0
	v_mbcnt_lo_u32_b32 v69, s90, 0
	v_mbcnt_lo_u32_b32 v70, s94, 0
	s_bcnt1_i32_b64 s93, s[70:71]
	s_add_i32 s4, s4, s93
	s_lshl1_add_u32 s85, s4, s52
	v_mbcnt_hi_u32_b32 v67, s71, v67
	s_bcnt1_i32_b64 s93, s[88:89]
	s_add_i32 s4, s4, s93
	s_lshl1_add_u32 s86, s4, s52
	v_mbcnt_hi_u32_b32 v68, s89, v68
	s_bcnt1_i32_b64 s93, s[90:91]
	s_add_i32 s4, s4, s93
	s_lshl1_add_u32 s15, s4, s52
	v_mbcnt_hi_u32_b32 v69, s91, v69
	s_bcnt1_i32_b64 s93, s[94:95]
	s_add_i32 s4, s4, s93
	v_mbcnt_hi_u32_b32 v70, s95, v70
	v_lshl_add_u32 v67, v67, 1, s32
	v_lshl_add_u32 v68, v68, 1, s85
	v_lshl_add_u32 v69, v69, 1, s86
	v_lshl_add_u32 v70, v70, 1, s15
	s_mov_b64 exec, s[70:71]
	ds_write_b16 v67, v167 offset:32768
	s_mov_b64 exec, s[88:89]
	ds_write_b16 v68, v168 offset:32768
	s_mov_b64 exec, s[90:91]
	ds_write_b16 v69, v169 offset:32768
	s_mov_b64 exec, s[94:95]
	ds_write_b16 v70, v170 offset:32768
	s_mov_b64 exec, s[30:31]
	v_cmp_gt_u32_sdwa s[70:71], v36, v66 src0_sel:WORD_0 src1_sel:DWORD
	v_cmp_gt_u32_sdwa s[88:89], v36, v66 src0_sel:WORD_1 src1_sel:DWORD
	v_cmp_gt_u32_sdwa s[90:91], v37, v66 src0_sel:WORD_0 src1_sel:DWORD
	v_cmp_gt_u32_sdwa s[94:95], v37, v66 src0_sel:WORD_1 src1_sel:DWORD
	s_lshl1_add_u32 s32, s4, s52
	v_mbcnt_lo_u32_b32 v67, s70, 0
	v_mbcnt_lo_u32_b32 v68, s88, 0
	v_mbcnt_lo_u32_b32 v69, s90, 0
	v_mbcnt_lo_u32_b32 v70, s94, 0
	s_bcnt1_i32_b64 s93, s[70:71]
	s_add_i32 s4, s4, s93
	s_lshl1_add_u32 s85, s4, s52
	v_mbcnt_hi_u32_b32 v67, s71, v67
	s_bcnt1_i32_b64 s93, s[88:89]
	s_add_i32 s4, s4, s93
	s_lshl1_add_u32 s86, s4, s52
	v_mbcnt_hi_u32_b32 v68, s89, v68
	s_bcnt1_i32_b64 s93, s[90:91]
	s_add_i32 s4, s4, s93
	s_lshl1_add_u32 s15, s4, s52
	v_mbcnt_hi_u32_b32 v69, s91, v69
	s_bcnt1_i32_b64 s93, s[94:95]
	s_add_i32 s4, s4, s93
	v_mbcnt_hi_u32_b32 v70, s95, v70
	v_lshl_add_u32 v67, v67, 1, s32
	v_lshl_add_u32 v68, v68, 1, s85
	v_lshl_add_u32 v69, v69, 1, s86
	v_lshl_add_u32 v70, v70, 1, s15
	s_mov_b64 exec, s[70:71]
	ds_write_b16 v67, v171 offset:32768
	s_mov_b64 exec, s[88:89]
	ds_write_b16 v68, v172 offset:32768
	s_mov_b64 exec, s[90:91]
	ds_write_b16 v69, v173 offset:32768
	s_mov_b64 exec, s[94:95]
	ds_write_b16 v70, v174 offset:32768
	s_mov_b64 exec, s[30:31]
	s_cmp_gt_i32 s14, 7
	s_cselect_b64 s[58:59], -1, 0
	s_cmp_lt_i32 s14, 8
	s_cbranch_scc1 .LBB0_1284
.LBB0_1394:
	s_mov_b64 s[30:31], exec
	v_cmp_gt_u32_sdwa s[70:71], v22, v66 src0_sel:WORD_0 src1_sel:DWORD
	v_cmp_gt_u32_sdwa s[88:89], v22, v66 src0_sel:WORD_1 src1_sel:DWORD
	v_cmp_gt_u32_sdwa s[90:91], v23, v66 src0_sel:WORD_0 src1_sel:DWORD
	v_cmp_gt_u32_sdwa s[94:95], v23, v66 src0_sel:WORD_1 src1_sel:DWORD
	s_lshl1_add_u32 s32, s4, s52
	v_mbcnt_lo_u32_b32 v67, s70, 0
	v_mbcnt_lo_u32_b32 v68, s88, 0
	v_mbcnt_lo_u32_b32 v69, s90, 0
	v_mbcnt_lo_u32_b32 v70, s94, 0
	s_bcnt1_i32_b64 s93, s[70:71]
	s_add_i32 s4, s4, s93
	s_lshl1_add_u32 s85, s4, s52
	v_mbcnt_hi_u32_b32 v67, s71, v67
	s_bcnt1_i32_b64 s93, s[88:89]
	s_add_i32 s4, s4, s93
	s_lshl1_add_u32 s86, s4, s52
	v_mbcnt_hi_u32_b32 v68, s89, v68
	s_bcnt1_i32_b64 s93, s[90:91]
	s_add_i32 s4, s4, s93
	s_lshl1_add_u32 s15, s4, s52
	v_mbcnt_hi_u32_b32 v69, s91, v69
	s_bcnt1_i32_b64 s93, s[94:95]
	s_add_i32 s4, s4, s93
	v_mbcnt_hi_u32_b32 v70, s95, v70
	v_lshl_add_u32 v67, v67, 1, s32
	v_lshl_add_u32 v68, v68, 1, s85
	v_lshl_add_u32 v69, v69, 1, s86
	v_lshl_add_u32 v70, v70, 1, s15
	s_mov_b64 exec, s[70:71]
	ds_write_b16 v67, v175 offset:32768
	s_mov_b64 exec, s[88:89]
	ds_write_b16 v68, v176 offset:32768
	s_mov_b64 exec, s[90:91]
	ds_write_b16 v69, v177 offset:32768
	s_mov_b64 exec, s[94:95]
	ds_write_b16 v70, v178 offset:32768
	s_mov_b64 exec, s[30:31]
	v_cmp_gt_u32_sdwa s[70:71], v24, v66 src0_sel:WORD_0 src1_sel:DWORD
	v_cmp_gt_u32_sdwa s[88:89], v24, v66 src0_sel:WORD_1 src1_sel:DWORD
	v_cmp_gt_u32_sdwa s[90:91], v25, v66 src0_sel:WORD_0 src1_sel:DWORD
	v_cmp_gt_u32_sdwa s[94:95], v25, v66 src0_sel:WORD_1 src1_sel:DWORD
	s_lshl1_add_u32 s32, s4, s52
	v_mbcnt_lo_u32_b32 v67, s70, 0
	v_mbcnt_lo_u32_b32 v68, s88, 0
	v_mbcnt_lo_u32_b32 v69, s90, 0
	v_mbcnt_lo_u32_b32 v70, s94, 0
	s_bcnt1_i32_b64 s93, s[70:71]
	s_add_i32 s4, s4, s93
	s_lshl1_add_u32 s85, s4, s52
	v_mbcnt_hi_u32_b32 v67, s71, v67
	s_bcnt1_i32_b64 s93, s[88:89]
	s_add_i32 s4, s4, s93
	s_lshl1_add_u32 s86, s4, s52
	v_mbcnt_hi_u32_b32 v68, s89, v68
	s_bcnt1_i32_b64 s93, s[90:91]
	s_add_i32 s4, s4, s93
	s_lshl1_add_u32 s15, s4, s52
	v_mbcnt_hi_u32_b32 v69, s91, v69
	s_bcnt1_i32_b64 s93, s[94:95]
	s_add_i32 s4, s4, s93
	v_mbcnt_hi_u32_b32 v70, s95, v70
	v_lshl_add_u32 v67, v67, 1, s32
	v_lshl_add_u32 v68, v68, 1, s85
	v_lshl_add_u32 v69, v69, 1, s86
	v_lshl_add_u32 v70, v70, 1, s15
	s_mov_b64 exec, s[70:71]
	ds_write_b16 v67, v179 offset:32768
	s_mov_b64 exec, s[88:89]
	ds_write_b16 v68, v180 offset:32768
	s_mov_b64 exec, s[90:91]
	ds_write_b16 v69, v181 offset:32768
	s_mov_b64 exec, s[94:95]
	ds_write_b16 v70, v182 offset:32768
	s_mov_b64 exec, s[30:31]
	s_andn2_b64 vcc, exec, s[26:27]
	s_cbranch_vccnz .LBB0_1285
.LBB0_1411:
	s_mov_b64 s[30:31], exec
	v_cmp_gt_u32_sdwa s[70:71], v62, v66 src0_sel:WORD_0 src1_sel:DWORD
	v_cmp_gt_u32_sdwa s[88:89], v62, v66 src0_sel:WORD_1 src1_sel:DWORD
	v_cmp_gt_u32_sdwa s[90:91], v63, v66 src0_sel:WORD_0 src1_sel:DWORD
	v_cmp_gt_u32_sdwa s[94:95], v63, v66 src0_sel:WORD_1 src1_sel:DWORD
	s_lshl1_add_u32 s32, s4, s52
	v_mbcnt_lo_u32_b32 v67, s70, 0
	v_mbcnt_lo_u32_b32 v68, s88, 0
	v_mbcnt_lo_u32_b32 v69, s90, 0
	v_mbcnt_lo_u32_b32 v70, s94, 0
	s_bcnt1_i32_b64 s93, s[70:71]
	s_add_i32 s4, s4, s93
	s_lshl1_add_u32 s85, s4, s52
	v_mbcnt_hi_u32_b32 v67, s71, v67
	s_bcnt1_i32_b64 s93, s[88:89]
	s_add_i32 s4, s4, s93
	s_lshl1_add_u32 s86, s4, s52
	v_mbcnt_hi_u32_b32 v68, s89, v68
	s_bcnt1_i32_b64 s93, s[90:91]
	s_add_i32 s4, s4, s93
	s_lshl1_add_u32 s15, s4, s52
	v_mbcnt_hi_u32_b32 v69, s91, v69
	s_bcnt1_i32_b64 s93, s[94:95]
	s_add_i32 s4, s4, s93
	v_mbcnt_hi_u32_b32 v70, s95, v70
	v_lshl_add_u32 v67, v67, 1, s32
	v_lshl_add_u32 v68, v68, 1, s85
	v_lshl_add_u32 v69, v69, 1, s86
	v_lshl_add_u32 v70, v70, 1, s15
	s_mov_b64 exec, s[70:71]
	ds_write_b16 v67, v183 offset:32768
	s_mov_b64 exec, s[88:89]
	ds_write_b16 v68, v184 offset:32768
	s_mov_b64 exec, s[90:91]
	ds_write_b16 v69, v185 offset:32768
	s_mov_b64 exec, s[94:95]
	ds_write_b16 v70, v186 offset:32768
	s_mov_b64 exec, s[30:31]
	v_cmp_gt_u32_sdwa s[70:71], v64, v66 src0_sel:WORD_0 src1_sel:DWORD
	v_cmp_gt_u32_sdwa s[88:89], v64, v66 src0_sel:WORD_1 src1_sel:DWORD
	v_cmp_gt_u32_sdwa s[90:91], v65, v66 src0_sel:WORD_0 src1_sel:DWORD
	v_cmp_gt_u32_sdwa s[94:95], v65, v66 src0_sel:WORD_1 src1_sel:DWORD
	s_lshl1_add_u32 s32, s4, s52
	v_mbcnt_lo_u32_b32 v67, s70, 0
	v_mbcnt_lo_u32_b32 v68, s88, 0
	v_mbcnt_lo_u32_b32 v69, s90, 0
	v_mbcnt_lo_u32_b32 v70, s94, 0
	s_bcnt1_i32_b64 s93, s[70:71]
	s_add_i32 s4, s4, s93
	s_lshl1_add_u32 s85, s4, s52
	v_mbcnt_hi_u32_b32 v67, s71, v67
	s_bcnt1_i32_b64 s93, s[88:89]
	s_add_i32 s4, s4, s93
	s_lshl1_add_u32 s86, s4, s52
	v_mbcnt_hi_u32_b32 v68, s89, v68
	s_bcnt1_i32_b64 s93, s[90:91]
	s_add_i32 s4, s4, s93
	s_lshl1_add_u32 s15, s4, s52
	v_mbcnt_hi_u32_b32 v69, s91, v69
	s_bcnt1_i32_b64 s93, s[94:95]
	s_add_i32 s4, s4, s93
	v_mbcnt_hi_u32_b32 v70, s95, v70
	v_lshl_add_u32 v67, v67, 1, s32
	v_lshl_add_u32 v68, v68, 1, s85
	v_lshl_add_u32 v69, v69, 1, s86
	v_lshl_add_u32 v70, v70, 1, s15
	s_mov_b64 exec, s[70:71]
	ds_write_b16 v67, v187 offset:32768
	s_mov_b64 exec, s[88:89]
	ds_write_b16 v68, v188 offset:32768
	s_mov_b64 exec, s[90:91]
	ds_write_b16 v69, v189 offset:32768
	s_mov_b64 exec, s[94:95]
	ds_write_b16 v70, v190 offset:32768
	s_mov_b64 exec, s[30:31]
	s_cmp_gt_i32 s14, 9
	s_cselect_b64 s[44:45], -1, 0
	s_cmp_lt_i32 s14, 10
	s_cbranch_scc1 .LBB0_1286
.LBB0_1428:
	s_mov_b64 s[30:31], exec
	v_cmp_gt_u32_sdwa s[70:71], v54, v66 src0_sel:WORD_0 src1_sel:DWORD
	v_cmp_gt_u32_sdwa s[88:89], v54, v66 src0_sel:WORD_1 src1_sel:DWORD
	v_cmp_gt_u32_sdwa s[90:91], v55, v66 src0_sel:WORD_0 src1_sel:DWORD
	v_cmp_gt_u32_sdwa s[94:95], v55, v66 src0_sel:WORD_1 src1_sel:DWORD
	s_lshl1_add_u32 s32, s4, s52
	v_mbcnt_lo_u32_b32 v67, s70, 0
	v_mbcnt_lo_u32_b32 v68, s88, 0
	v_mbcnt_lo_u32_b32 v69, s90, 0
	v_mbcnt_lo_u32_b32 v70, s94, 0
	s_bcnt1_i32_b64 s93, s[70:71]
	s_add_i32 s4, s4, s93
	s_lshl1_add_u32 s85, s4, s52
	v_mbcnt_hi_u32_b32 v67, s71, v67
	s_bcnt1_i32_b64 s93, s[88:89]
	s_add_i32 s4, s4, s93
	s_lshl1_add_u32 s86, s4, s52
	v_mbcnt_hi_u32_b32 v68, s89, v68
	s_bcnt1_i32_b64 s93, s[90:91]
	s_add_i32 s4, s4, s93
	s_lshl1_add_u32 s15, s4, s52
	v_mbcnt_hi_u32_b32 v69, s91, v69
	s_bcnt1_i32_b64 s93, s[94:95]
	s_add_i32 s4, s4, s93
	v_mbcnt_hi_u32_b32 v70, s95, v70
	v_lshl_add_u32 v67, v67, 1, s32
	v_lshl_add_u32 v68, v68, 1, s85
	v_lshl_add_u32 v69, v69, 1, s86
	v_lshl_add_u32 v70, v70, 1, s15
	s_mov_b64 exec, s[70:71]
	ds_write_b16 v67, v191 offset:32768
	s_mov_b64 exec, s[88:89]
	ds_write_b16 v68, v192 offset:32768
	s_mov_b64 exec, s[90:91]
	ds_write_b16 v69, v193 offset:32768
	s_mov_b64 exec, s[94:95]
	ds_write_b16 v70, v194 offset:32768
	s_mov_b64 exec, s[30:31]
	v_cmp_gt_u32_sdwa s[70:71], v56, v66 src0_sel:WORD_0 src1_sel:DWORD
	v_cmp_gt_u32_sdwa s[88:89], v56, v66 src0_sel:WORD_1 src1_sel:DWORD
	v_cmp_gt_u32_sdwa s[90:91], v57, v66 src0_sel:WORD_0 src1_sel:DWORD
	v_cmp_gt_u32_sdwa s[94:95], v57, v66 src0_sel:WORD_1 src1_sel:DWORD
	s_lshl1_add_u32 s32, s4, s52
	v_mbcnt_lo_u32_b32 v67, s70, 0
	v_mbcnt_lo_u32_b32 v68, s88, 0
	v_mbcnt_lo_u32_b32 v69, s90, 0
	v_mbcnt_lo_u32_b32 v70, s94, 0
	s_bcnt1_i32_b64 s93, s[70:71]
	s_add_i32 s4, s4, s93
	s_lshl1_add_u32 s85, s4, s52
	v_mbcnt_hi_u32_b32 v67, s71, v67
	s_bcnt1_i32_b64 s93, s[88:89]
	s_add_i32 s4, s4, s93
	s_lshl1_add_u32 s86, s4, s52
	v_mbcnt_hi_u32_b32 v68, s89, v68
	s_bcnt1_i32_b64 s93, s[90:91]
	s_add_i32 s4, s4, s93
	s_lshl1_add_u32 s15, s4, s52
	v_mbcnt_hi_u32_b32 v69, s91, v69
	s_bcnt1_i32_b64 s93, s[94:95]
	s_add_i32 s4, s4, s93
	v_mbcnt_hi_u32_b32 v70, s95, v70
	v_lshl_add_u32 v67, v67, 1, s32
	v_lshl_add_u32 v68, v68, 1, s85
	v_lshl_add_u32 v69, v69, 1, s86
	v_lshl_add_u32 v70, v70, 1, s15
	s_mov_b64 exec, s[70:71]
	ds_write_b16 v67, v195 offset:32768
	s_mov_b64 exec, s[88:89]
	ds_write_b16 v68, v196 offset:32768
	s_mov_b64 exec, s[90:91]
	ds_write_b16 v69, v197 offset:32768
	s_mov_b64 exec, s[94:95]
	ds_write_b16 v70, v198 offset:32768
	s_mov_b64 exec, s[30:31]
	s_cmp_gt_i32 s14, 10
	s_cselect_b64 s[40:41], -1, 0
	s_cmp_lt_i32 s14, 11
	s_cbranch_scc1 .LBB0_1287
.LBB0_1445:
	s_mov_b64 s[30:31], exec
	v_cmp_gt_u32_sdwa s[70:71], v42, v66 src0_sel:WORD_0 src1_sel:DWORD
	v_cmp_gt_u32_sdwa s[88:89], v42, v66 src0_sel:WORD_1 src1_sel:DWORD
	v_cmp_gt_u32_sdwa s[90:91], v43, v66 src0_sel:WORD_0 src1_sel:DWORD
	v_cmp_gt_u32_sdwa s[94:95], v43, v66 src0_sel:WORD_1 src1_sel:DWORD
	s_lshl1_add_u32 s32, s4, s52
	v_mbcnt_lo_u32_b32 v67, s70, 0
	v_mbcnt_lo_u32_b32 v68, s88, 0
	v_mbcnt_lo_u32_b32 v69, s90, 0
	v_mbcnt_lo_u32_b32 v70, s94, 0
	s_bcnt1_i32_b64 s93, s[70:71]
	s_add_i32 s4, s4, s93
	s_lshl1_add_u32 s85, s4, s52
	v_mbcnt_hi_u32_b32 v67, s71, v67
	s_bcnt1_i32_b64 s93, s[88:89]
	s_add_i32 s4, s4, s93
	s_lshl1_add_u32 s86, s4, s52
	v_mbcnt_hi_u32_b32 v68, s89, v68
	s_bcnt1_i32_b64 s93, s[90:91]
	s_add_i32 s4, s4, s93
	s_lshl1_add_u32 s15, s4, s52
	v_mbcnt_hi_u32_b32 v69, s91, v69
	s_bcnt1_i32_b64 s93, s[94:95]
	s_add_i32 s4, s4, s93
	v_mbcnt_hi_u32_b32 v70, s95, v70
	v_lshl_add_u32 v67, v67, 1, s32
	v_lshl_add_u32 v68, v68, 1, s85
	v_lshl_add_u32 v69, v69, 1, s86
	v_lshl_add_u32 v70, v70, 1, s15
	s_mov_b64 exec, s[70:71]
	ds_write_b16 v67, v199 offset:32768
	s_mov_b64 exec, s[88:89]
	ds_write_b16 v68, v200 offset:32768
	s_mov_b64 exec, s[90:91]
	ds_write_b16 v69, v201 offset:32768
	s_mov_b64 exec, s[94:95]
	ds_write_b16 v70, v202 offset:32768
	s_mov_b64 exec, s[30:31]
	v_cmp_gt_u32_sdwa s[70:71], v44, v66 src0_sel:WORD_0 src1_sel:DWORD
	v_cmp_gt_u32_sdwa s[88:89], v44, v66 src0_sel:WORD_1 src1_sel:DWORD
	v_cmp_gt_u32_sdwa s[90:91], v45, v66 src0_sel:WORD_0 src1_sel:DWORD
	v_cmp_gt_u32_sdwa s[94:95], v45, v66 src0_sel:WORD_1 src1_sel:DWORD
	s_lshl1_add_u32 s32, s4, s52
	v_mbcnt_lo_u32_b32 v67, s70, 0
	v_mbcnt_lo_u32_b32 v68, s88, 0
	v_mbcnt_lo_u32_b32 v69, s90, 0
	v_mbcnt_lo_u32_b32 v70, s94, 0
	s_bcnt1_i32_b64 s93, s[70:71]
	s_add_i32 s4, s4, s93
	s_lshl1_add_u32 s85, s4, s52
	v_mbcnt_hi_u32_b32 v67, s71, v67
	s_bcnt1_i32_b64 s93, s[88:89]
	s_add_i32 s4, s4, s93
	s_lshl1_add_u32 s86, s4, s52
	v_mbcnt_hi_u32_b32 v68, s89, v68
	s_bcnt1_i32_b64 s93, s[90:91]
	s_add_i32 s4, s4, s93
	s_lshl1_add_u32 s15, s4, s52
	v_mbcnt_hi_u32_b32 v69, s91, v69
	s_bcnt1_i32_b64 s93, s[94:95]
	s_add_i32 s4, s4, s93
	v_mbcnt_hi_u32_b32 v70, s95, v70
	v_lshl_add_u32 v67, v67, 1, s32
	v_lshl_add_u32 v68, v68, 1, s85
	v_lshl_add_u32 v69, v69, 1, s86
	v_lshl_add_u32 v70, v70, 1, s15
	s_mov_b64 exec, s[70:71]
	ds_write_b16 v67, v203 offset:32768
	s_mov_b64 exec, s[88:89]
	ds_write_b16 v68, v204 offset:32768
	s_mov_b64 exec, s[90:91]
	ds_write_b16 v69, v205 offset:32768
	s_mov_b64 exec, s[94:95]
	ds_write_b16 v70, v206 offset:32768
	s_mov_b64 exec, s[30:31]
	s_cmp_gt_i32 s14, 11
	s_cselect_b64 s[38:39], -1, 0
	s_cmp_lt_i32 s14, 12
	s_cbranch_scc1 .LBB0_1288
.LBB0_1462:
	s_mov_b64 s[30:31], exec
	v_cmp_gt_u32_sdwa s[70:71], v30, v66 src0_sel:WORD_0 src1_sel:DWORD
	v_cmp_gt_u32_sdwa s[88:89], v30, v66 src0_sel:WORD_1 src1_sel:DWORD
	v_cmp_gt_u32_sdwa s[90:91], v31, v66 src0_sel:WORD_0 src1_sel:DWORD
	v_cmp_gt_u32_sdwa s[94:95], v31, v66 src0_sel:WORD_1 src1_sel:DWORD
	s_lshl1_add_u32 s32, s4, s52
	v_mbcnt_lo_u32_b32 v67, s70, 0
	v_mbcnt_lo_u32_b32 v68, s88, 0
	v_mbcnt_lo_u32_b32 v69, s90, 0
	v_mbcnt_lo_u32_b32 v70, s94, 0
	s_bcnt1_i32_b64 s93, s[70:71]
	s_add_i32 s4, s4, s93
	s_lshl1_add_u32 s85, s4, s52
	v_mbcnt_hi_u32_b32 v67, s71, v67
	s_bcnt1_i32_b64 s93, s[88:89]
	s_add_i32 s4, s4, s93
	s_lshl1_add_u32 s86, s4, s52
	v_mbcnt_hi_u32_b32 v68, s89, v68
	s_bcnt1_i32_b64 s93, s[90:91]
	s_add_i32 s4, s4, s93
	s_lshl1_add_u32 s15, s4, s52
	v_mbcnt_hi_u32_b32 v69, s91, v69
	s_bcnt1_i32_b64 s93, s[94:95]
	s_add_i32 s4, s4, s93
	v_mbcnt_hi_u32_b32 v70, s95, v70
	v_lshl_add_u32 v67, v67, 1, s32
	v_lshl_add_u32 v68, v68, 1, s85
	v_lshl_add_u32 v69, v69, 1, s86
	v_lshl_add_u32 v70, v70, 1, s15
	s_mov_b64 exec, s[70:71]
	ds_write_b16 v67, v207 offset:32768
	s_mov_b64 exec, s[88:89]
	ds_write_b16 v68, v208 offset:32768
	s_mov_b64 exec, s[90:91]
	ds_write_b16 v69, v209 offset:32768
	s_mov_b64 exec, s[94:95]
	ds_write_b16 v70, v210 offset:32768
	s_mov_b64 exec, s[30:31]
	v_cmp_gt_u32_sdwa s[70:71], v32, v66 src0_sel:WORD_0 src1_sel:DWORD
	v_cmp_gt_u32_sdwa s[88:89], v32, v66 src0_sel:WORD_1 src1_sel:DWORD
	v_cmp_gt_u32_sdwa s[90:91], v33, v66 src0_sel:WORD_0 src1_sel:DWORD
	v_cmp_gt_u32_sdwa s[94:95], v33, v66 src0_sel:WORD_1 src1_sel:DWORD
	s_lshl1_add_u32 s32, s4, s52
	v_mbcnt_lo_u32_b32 v67, s70, 0
	v_mbcnt_lo_u32_b32 v68, s88, 0
	v_mbcnt_lo_u32_b32 v69, s90, 0
	v_mbcnt_lo_u32_b32 v70, s94, 0
	s_bcnt1_i32_b64 s93, s[70:71]
	s_add_i32 s4, s4, s93
	s_lshl1_add_u32 s85, s4, s52
	v_mbcnt_hi_u32_b32 v67, s71, v67
	s_bcnt1_i32_b64 s93, s[88:89]
	s_add_i32 s4, s4, s93
	s_lshl1_add_u32 s86, s4, s52
	v_mbcnt_hi_u32_b32 v68, s89, v68
	s_bcnt1_i32_b64 s93, s[90:91]
	s_add_i32 s4, s4, s93
	s_lshl1_add_u32 s15, s4, s52
	v_mbcnt_hi_u32_b32 v69, s91, v69
	s_bcnt1_i32_b64 s93, s[94:95]
	s_add_i32 s4, s4, s93
	v_mbcnt_hi_u32_b32 v70, s95, v70
	v_lshl_add_u32 v67, v67, 1, s32
	v_lshl_add_u32 v68, v68, 1, s85
	v_lshl_add_u32 v69, v69, 1, s86
	v_lshl_add_u32 v70, v70, 1, s15
	s_mov_b64 exec, s[70:71]
	ds_write_b16 v67, v211 offset:32768
	s_mov_b64 exec, s[88:89]
	ds_write_b16 v68, v212 offset:32768
	s_mov_b64 exec, s[90:91]
	ds_write_b16 v69, v213 offset:32768
	s_mov_b64 exec, s[94:95]
	ds_write_b16 v70, v214 offset:32768
	s_mov_b64 exec, s[30:31]
	s_andn2_b64 vcc, exec, s[2:3]
	s_cbranch_vccnz .LBB0_1289
.LBB0_1479:
	s_mov_b64 s[30:31], exec
	v_cmp_gt_u32_sdwa s[70:71], v14, v66 src0_sel:WORD_0 src1_sel:DWORD
	v_cmp_gt_u32_sdwa s[88:89], v14, v66 src0_sel:WORD_1 src1_sel:DWORD
	v_cmp_gt_u32_sdwa s[90:91], v15, v66 src0_sel:WORD_0 src1_sel:DWORD
	v_cmp_gt_u32_sdwa s[94:95], v15, v66 src0_sel:WORD_1 src1_sel:DWORD
	s_lshl1_add_u32 s32, s4, s52
	v_mbcnt_lo_u32_b32 v67, s70, 0
	v_mbcnt_lo_u32_b32 v68, s88, 0
	v_mbcnt_lo_u32_b32 v69, s90, 0
	v_mbcnt_lo_u32_b32 v70, s94, 0
	s_bcnt1_i32_b64 s93, s[70:71]
	s_add_i32 s4, s4, s93
	s_lshl1_add_u32 s85, s4, s52
	v_mbcnt_hi_u32_b32 v67, s71, v67
	s_bcnt1_i32_b64 s93, s[88:89]
	s_add_i32 s4, s4, s93
	s_lshl1_add_u32 s86, s4, s52
	v_mbcnt_hi_u32_b32 v68, s89, v68
	s_bcnt1_i32_b64 s93, s[90:91]
	s_add_i32 s4, s4, s93
	s_lshl1_add_u32 s15, s4, s52
	v_mbcnt_hi_u32_b32 v69, s91, v69
	s_bcnt1_i32_b64 s93, s[94:95]
	s_add_i32 s4, s4, s93
	v_mbcnt_hi_u32_b32 v70, s95, v70
	v_lshl_add_u32 v67, v67, 1, s32
	v_lshl_add_u32 v68, v68, 1, s85
	v_lshl_add_u32 v69, v69, 1, s86
	v_lshl_add_u32 v70, v70, 1, s15
	s_mov_b64 exec, s[70:71]
	ds_write_b16 v67, v215 offset:32768
	s_mov_b64 exec, s[88:89]
	ds_write_b16 v68, v216 offset:32768
	s_mov_b64 exec, s[90:91]
	ds_write_b16 v69, v217 offset:32768
	s_mov_b64 exec, s[94:95]
	ds_write_b16 v70, v218 offset:32768
	s_mov_b64 exec, s[30:31]
	v_cmp_gt_u32_sdwa s[70:71], v16, v66 src0_sel:WORD_0 src1_sel:DWORD
	v_cmp_gt_u32_sdwa s[88:89], v16, v66 src0_sel:WORD_1 src1_sel:DWORD
	v_cmp_gt_u32_sdwa s[90:91], v17, v66 src0_sel:WORD_0 src1_sel:DWORD
	v_cmp_gt_u32_sdwa s[94:95], v17, v66 src0_sel:WORD_1 src1_sel:DWORD
	s_lshl1_add_u32 s32, s4, s52
	v_mbcnt_lo_u32_b32 v67, s70, 0
	v_mbcnt_lo_u32_b32 v68, s88, 0
	v_mbcnt_lo_u32_b32 v69, s90, 0
	v_mbcnt_lo_u32_b32 v70, s94, 0
	s_bcnt1_i32_b64 s93, s[70:71]
	s_add_i32 s4, s4, s93
	s_lshl1_add_u32 s85, s4, s52
	v_mbcnt_hi_u32_b32 v67, s71, v67
	s_bcnt1_i32_b64 s93, s[88:89]
	s_add_i32 s4, s4, s93
	s_lshl1_add_u32 s86, s4, s52
	v_mbcnt_hi_u32_b32 v68, s89, v68
	s_bcnt1_i32_b64 s93, s[90:91]
	s_add_i32 s4, s4, s93
	s_lshl1_add_u32 s15, s4, s52
	v_mbcnt_hi_u32_b32 v69, s91, v69
	s_bcnt1_i32_b64 s93, s[94:95]
	s_add_i32 s4, s4, s93
	v_mbcnt_hi_u32_b32 v70, s95, v70
	v_lshl_add_u32 v67, v67, 1, s32
	v_lshl_add_u32 v68, v68, 1, s85
	v_lshl_add_u32 v69, v69, 1, s86
	v_lshl_add_u32 v70, v70, 1, s15
	s_mov_b64 exec, s[70:71]
	ds_write_b16 v67, v219 offset:32768
	s_mov_b64 exec, s[88:89]
	ds_write_b16 v68, v220 offset:32768
	s_mov_b64 exec, s[90:91]
	ds_write_b16 v69, v221 offset:32768
	s_mov_b64 exec, s[94:95]
	ds_write_b16 v70, v222 offset:32768
	s_mov_b64 exec, s[30:31]
	s_cmp_gt_i32 s14, 13
	s_cselect_b64 s[36:37], -1, 0
	s_cmp_lt_i32 s14, 14
	s_cbranch_scc1 .LBB0_1290
.LBB0_1496:
	s_mov_b64 s[30:31], exec
	v_cmp_gt_u32_sdwa s[70:71], v10, v66 src0_sel:WORD_0 src1_sel:DWORD
	v_cmp_gt_u32_sdwa s[88:89], v10, v66 src0_sel:WORD_1 src1_sel:DWORD
	v_cmp_gt_u32_sdwa s[90:91], v11, v66 src0_sel:WORD_0 src1_sel:DWORD
	v_cmp_gt_u32_sdwa s[94:95], v11, v66 src0_sel:WORD_1 src1_sel:DWORD
	s_lshl1_add_u32 s32, s4, s52
	v_mbcnt_lo_u32_b32 v67, s70, 0
	v_mbcnt_lo_u32_b32 v68, s88, 0
	v_mbcnt_lo_u32_b32 v69, s90, 0
	v_mbcnt_lo_u32_b32 v70, s94, 0
	s_bcnt1_i32_b64 s93, s[70:71]
	s_add_i32 s4, s4, s93
	s_lshl1_add_u32 s85, s4, s52
	v_mbcnt_hi_u32_b32 v67, s71, v67
	s_bcnt1_i32_b64 s93, s[88:89]
	s_add_i32 s4, s4, s93
	s_lshl1_add_u32 s86, s4, s52
	v_mbcnt_hi_u32_b32 v68, s89, v68
	s_bcnt1_i32_b64 s93, s[90:91]
	s_add_i32 s4, s4, s93
	s_lshl1_add_u32 s15, s4, s52
	v_mbcnt_hi_u32_b32 v69, s91, v69
	s_bcnt1_i32_b64 s93, s[94:95]
	s_add_i32 s4, s4, s93
	v_mbcnt_hi_u32_b32 v70, s95, v70
	v_lshl_add_u32 v67, v67, 1, s32
	v_lshl_add_u32 v68, v68, 1, s85
	v_lshl_add_u32 v69, v69, 1, s86
	v_lshl_add_u32 v70, v70, 1, s15
	s_mov_b64 exec, s[70:71]
	ds_write_b16 v67, v223 offset:32768
	s_mov_b64 exec, s[88:89]
	ds_write_b16 v68, v224 offset:32768
	s_mov_b64 exec, s[90:91]
	ds_write_b16 v69, v225 offset:32768
	s_mov_b64 exec, s[94:95]
	ds_write_b16 v70, v226 offset:32768
	s_mov_b64 exec, s[30:31]
	v_cmp_gt_u32_sdwa s[70:71], v12, v66 src0_sel:WORD_0 src1_sel:DWORD
	v_cmp_gt_u32_sdwa s[88:89], v12, v66 src0_sel:WORD_1 src1_sel:DWORD
	v_cmp_gt_u32_sdwa s[90:91], v13, v66 src0_sel:WORD_0 src1_sel:DWORD
	v_cmp_gt_u32_sdwa s[94:95], v13, v66 src0_sel:WORD_1 src1_sel:DWORD
	s_lshl1_add_u32 s32, s4, s52
	v_mbcnt_lo_u32_b32 v67, s70, 0
	v_mbcnt_lo_u32_b32 v68, s88, 0
	v_mbcnt_lo_u32_b32 v69, s90, 0
	v_mbcnt_lo_u32_b32 v70, s94, 0
	s_bcnt1_i32_b64 s93, s[70:71]
	s_add_i32 s4, s4, s93
	s_lshl1_add_u32 s85, s4, s52
	v_mbcnt_hi_u32_b32 v67, s71, v67
	s_bcnt1_i32_b64 s93, s[88:89]
	s_add_i32 s4, s4, s93
	s_lshl1_add_u32 s86, s4, s52
	v_mbcnt_hi_u32_b32 v68, s89, v68
	s_bcnt1_i32_b64 s93, s[90:91]
	s_add_i32 s4, s4, s93
	s_lshl1_add_u32 s15, s4, s52
	v_mbcnt_hi_u32_b32 v69, s91, v69
	s_bcnt1_i32_b64 s93, s[94:95]
	s_add_i32 s4, s4, s93
	v_mbcnt_hi_u32_b32 v70, s95, v70
	v_lshl_add_u32 v67, v67, 1, s32
	v_lshl_add_u32 v68, v68, 1, s85
	v_lshl_add_u32 v69, v69, 1, s86
	v_lshl_add_u32 v70, v70, 1, s15
	s_mov_b64 exec, s[70:71]
	ds_write_b16 v67, v227 offset:32768
	s_mov_b64 exec, s[88:89]
	ds_write_b16 v68, v228 offset:32768
	s_mov_b64 exec, s[90:91]
	ds_write_b16 v69, v229 offset:32768
	s_mov_b64 exec, s[94:95]
	ds_write_b16 v70, v230 offset:32768
	s_mov_b64 exec, s[30:31]
	s_cmp_gt_i32 s14, 14
	s_cselect_b64 s[34:35], -1, 0
	s_cmp_lt_i32 s14, 15
	s_cbranch_scc1 .LBB0_1291
.LBB0_1513:
	s_mov_b64 s[30:31], exec
	v_cmp_gt_u32_sdwa s[70:71], v6, v66 src0_sel:WORD_0 src1_sel:DWORD
	v_cmp_gt_u32_sdwa s[88:89], v6, v66 src0_sel:WORD_1 src1_sel:DWORD
	v_cmp_gt_u32_sdwa s[90:91], v7, v66 src0_sel:WORD_0 src1_sel:DWORD
	v_cmp_gt_u32_sdwa s[94:95], v7, v66 src0_sel:WORD_1 src1_sel:DWORD
	s_lshl1_add_u32 s32, s4, s52
	v_mbcnt_lo_u32_b32 v67, s70, 0
	v_mbcnt_lo_u32_b32 v68, s88, 0
	v_mbcnt_lo_u32_b32 v69, s90, 0
	v_mbcnt_lo_u32_b32 v70, s94, 0
	s_bcnt1_i32_b64 s93, s[70:71]
	s_add_i32 s4, s4, s93
	s_lshl1_add_u32 s85, s4, s52
	v_mbcnt_hi_u32_b32 v67, s71, v67
	s_bcnt1_i32_b64 s93, s[88:89]
	s_add_i32 s4, s4, s93
	s_lshl1_add_u32 s86, s4, s52
	v_mbcnt_hi_u32_b32 v68, s89, v68
	s_bcnt1_i32_b64 s93, s[90:91]
	s_add_i32 s4, s4, s93
	s_lshl1_add_u32 s15, s4, s52
	v_mbcnt_hi_u32_b32 v69, s91, v69
	s_bcnt1_i32_b64 s93, s[94:95]
	s_add_i32 s4, s4, s93
	v_mbcnt_hi_u32_b32 v70, s95, v70
	v_lshl_add_u32 v67, v67, 1, s32
	v_lshl_add_u32 v68, v68, 1, s85
	v_lshl_add_u32 v69, v69, 1, s86
	v_lshl_add_u32 v70, v70, 1, s15
	s_mov_b64 exec, s[70:71]
	ds_write_b16 v67, v231 offset:32768
	s_mov_b64 exec, s[88:89]
	ds_write_b16 v68, v232 offset:32768
	s_mov_b64 exec, s[90:91]
	ds_write_b16 v69, v233 offset:32768
	s_mov_b64 exec, s[94:95]
	ds_write_b16 v70, v234 offset:32768
	s_mov_b64 exec, s[30:31]
	v_cmp_gt_u32_sdwa s[70:71], v8, v66 src0_sel:WORD_0 src1_sel:DWORD
	v_cmp_gt_u32_sdwa s[88:89], v8, v66 src0_sel:WORD_1 src1_sel:DWORD
	v_cmp_gt_u32_sdwa s[90:91], v9, v66 src0_sel:WORD_0 src1_sel:DWORD
	v_cmp_gt_u32_sdwa s[94:95], v9, v66 src0_sel:WORD_1 src1_sel:DWORD
	s_lshl1_add_u32 s32, s4, s52
	v_mbcnt_lo_u32_b32 v67, s70, 0
	v_mbcnt_lo_u32_b32 v68, s88, 0
	v_mbcnt_lo_u32_b32 v69, s90, 0
	v_mbcnt_lo_u32_b32 v70, s94, 0
	s_bcnt1_i32_b64 s93, s[70:71]
	s_add_i32 s4, s4, s93
	s_lshl1_add_u32 s85, s4, s52
	v_mbcnt_hi_u32_b32 v67, s71, v67
	s_bcnt1_i32_b64 s93, s[88:89]
	s_add_i32 s4, s4, s93
	s_lshl1_add_u32 s86, s4, s52
	v_mbcnt_hi_u32_b32 v68, s89, v68
	s_bcnt1_i32_b64 s93, s[90:91]
	s_add_i32 s4, s4, s93
	s_lshl1_add_u32 s15, s4, s52
	v_mbcnt_hi_u32_b32 v69, s91, v69
	s_bcnt1_i32_b64 s93, s[94:95]
	s_add_i32 s4, s4, s93
	v_mbcnt_hi_u32_b32 v70, s95, v70
	v_lshl_add_u32 v67, v67, 1, s32
	v_lshl_add_u32 v68, v68, 1, s85
	v_lshl_add_u32 v69, v69, 1, s86
	v_lshl_add_u32 v70, v70, 1, s15
	s_mov_b64 exec, s[70:71]
	ds_write_b16 v67, v235 offset:32768
	s_mov_b64 exec, s[88:89]
	ds_write_b16 v68, v236 offset:32768
	s_mov_b64 exec, s[90:91]
	ds_write_b16 v69, v237 offset:32768
	s_mov_b64 exec, s[94:95]
	ds_write_b16 v70, v238 offset:32768
	s_mov_b64 exec, s[30:31]
	s_cmp_gt_i32 s14, 15
	s_cselect_b64 s[30:31], -1, 0
	s_cmp_lt_i32 s14, 16
	s_cbranch_scc1 .LBB0_1547
.LBB0_1530:
	s_mov_b64 vcc, exec
	v_cmp_gt_u32_sdwa s[70:71], v2, v66 src0_sel:WORD_0 src1_sel:DWORD
	v_cmp_gt_u32_sdwa s[88:89], v2, v66 src0_sel:WORD_1 src1_sel:DWORD
	v_cmp_gt_u32_sdwa s[90:91], v3, v66 src0_sel:WORD_0 src1_sel:DWORD
	v_cmp_gt_u32_sdwa s[94:95], v3, v66 src0_sel:WORD_1 src1_sel:DWORD
	s_lshl1_add_u32 s32, s4, s52
	v_mbcnt_lo_u32_b32 v67, s70, 0
	v_mbcnt_lo_u32_b32 v68, s88, 0
	v_mbcnt_lo_u32_b32 v69, s90, 0
	v_mbcnt_lo_u32_b32 v70, s94, 0
	s_bcnt1_i32_b64 s93, s[70:71]
	s_add_i32 s4, s4, s93
	s_lshl1_add_u32 s85, s4, s52
	v_mbcnt_hi_u32_b32 v67, s71, v67
	s_bcnt1_i32_b64 s93, s[88:89]
	s_add_i32 s4, s4, s93
	s_lshl1_add_u32 s86, s4, s52
	v_mbcnt_hi_u32_b32 v68, s89, v68
	s_bcnt1_i32_b64 s93, s[90:91]
	s_add_i32 s4, s4, s93
	s_lshl1_add_u32 s14, s4, s52
	v_mbcnt_hi_u32_b32 v69, s91, v69
	s_bcnt1_i32_b64 s93, s[94:95]
	s_add_i32 s4, s4, s93
	v_mbcnt_hi_u32_b32 v70, s95, v70
	v_lshl_add_u32 v67, v67, 1, s32
	v_lshl_add_u32 v68, v68, 1, s85
	v_lshl_add_u32 v69, v69, 1, s86
	v_lshl_add_u32 v70, v70, 1, s14
	s_mov_b64 exec, s[70:71]
	ds_write_b16 v67, v239 offset:32768
	s_mov_b64 exec, s[88:89]
	ds_write_b16 v68, v240 offset:32768
	s_mov_b64 exec, s[90:91]
	ds_write_b16 v69, v241 offset:32768
	s_mov_b64 exec, s[94:95]
	ds_write_b16 v70, v242 offset:32768
	s_mov_b64 exec, vcc
	v_cmp_gt_u32_sdwa s[70:71], v4, v66 src0_sel:WORD_0 src1_sel:DWORD
	v_cmp_gt_u32_sdwa s[88:89], v4, v66 src0_sel:WORD_1 src1_sel:DWORD
	v_cmp_gt_u32_sdwa s[90:91], v5, v66 src0_sel:WORD_0 src1_sel:DWORD
	v_cmp_gt_u32_sdwa s[94:95], v5, v66 src0_sel:WORD_1 src1_sel:DWORD
	s_lshl1_add_u32 s32, s4, s52
	v_mbcnt_lo_u32_b32 v67, s70, 0
	v_mbcnt_lo_u32_b32 v68, s88, 0
	v_mbcnt_lo_u32_b32 v69, s90, 0
	v_mbcnt_lo_u32_b32 v70, s94, 0
	s_bcnt1_i32_b64 s93, s[70:71]
	s_add_i32 s4, s4, s93
	s_lshl1_add_u32 s85, s4, s52
	v_mbcnt_hi_u32_b32 v67, s71, v67
	s_bcnt1_i32_b64 s93, s[88:89]
	s_add_i32 s4, s4, s93
	s_lshl1_add_u32 s86, s4, s52
	v_mbcnt_hi_u32_b32 v68, s89, v68
	s_bcnt1_i32_b64 s93, s[90:91]
	s_add_i32 s4, s4, s93
	s_lshl1_add_u32 s14, s4, s52
	v_mbcnt_hi_u32_b32 v69, s91, v69
	s_bcnt1_i32_b64 s93, s[94:95]
	s_add_i32 s4, s4, s93
	v_mbcnt_hi_u32_b32 v70, s95, v70
	v_lshl_add_u32 v67, v67, 1, s32
	v_lshl_add_u32 v68, v68, 1, s85
	v_lshl_add_u32 v69, v69, 1, s86
	v_lshl_add_u32 v70, v70, 1, s14
	s_mov_b64 exec, s[70:71]
	ds_write_b16 v67, v243 offset:32768
	s_mov_b64 exec, s[88:89]
	ds_write_b16 v68, v244 offset:32768
	s_mov_b64 exec, s[90:91]
	ds_write_b16 v69, v245 offset:32768
	s_mov_b64 exec, s[94:95]
	ds_write_b16 v70, v246 offset:32768
	s_mov_b64 exec, vcc
